# speedup vs baseline: 1.0039x; 1.0039x over previous
.LBB0_89:
	s_or_b64 exec, exec, s[8:9]
	v_mov_b32_e32 v3, 0
	v_lshlrev_b32_e32 v70, 4, v28
	s_and_saveexec_b64 s[60:61], vcc
	s_cbranch_execz .LBB0_118
	s_mov_b64 s[92:93], s[14:15]
	v_lshl_add_u64 v[22:23], s[12:13], 0, v[2:3]
	s_waitcnt vmcnt(0)
	v_cndmask_b32_e64 v55, -1, v4, s[0:1]
	s_movk_i32 s0, 0x880
	v_mov_b32_e32 v2, 0x1dd00
	v_mad_u32_u24 v4, v80, s0, v2
	v_lshlrev_b32_e32 v2, 1, v1
	v_mov_b32_e32 v27, v3
	v_mbcnt_hi_u32_b32 v2, -1, v29
	v_lshl_add_u64 v[72:73], v[22:23], 0, v[26:27]
	v_and_b32_e32 v23, 64, v2
	v_xor_b32_e32 v22, 16, v2
	v_add_u32_e32 v23, 64, v23
	v_cmp_lt_i32_e32 vcc, v22, v23
	v_lshlrev_b32_e32 v88, 2, v28
	v_and_b32_e32 v24, 7, v0
	v_cndmask_b32_e32 v22, v2, v22, vcc
	v_lshlrev_b32_e32 v90, 2, v22
	v_xor_b32_e32 v22, 32, v2
	v_cmp_lt_i32_e32 vcc, v22, v23
	s_mov_b32 s24, 0x10000
	v_cndmask_b32_e32 v2, v2, v22, vcc
	v_lshlrev_b32_e32 v91, 2, v2
	v_lshrrev_b32_e32 v2, 2, v79
	v_mul_u32_u24_e32 v22, 0x88, v79
	v_add3_u32 v92, v4, v22, v1
	v_or_b32_e32 v2, v88, v2
	v_lshlrev_b32_e32 v22, 3, v0
	v_mul_u32_u24_e32 v2, 0x88, v2
	v_and_b32_e32 v22, 24, v22
	v_add3_u32 v93, v4, v2, v22
	v_lshlrev_b32_e32 v2, 5, v24
	v_or3_b32 v78, v2, v1, s24
	v_bfe_u32 v2, v0, 1, 2
	v_lshrrev_b32_e32 v89, 3, v79
	v_cmp_eq_u32_e64 s[6:7], 4, v24
	v_cmp_eq_u32_e64 s[8:9], 3, v24
	v_cmp_eq_u32_e64 s[10:11], 2, v24
	v_cmp_eq_u32_e64 s[12:13], 1, v24
	v_cmp_eq_u32_e64 s[14:15], 0, v24
	v_cmp_eq_u32_e64 s[16:17], 7, v24
	v_cmp_eq_u32_e64 s[18:19], 6, v24
	v_cmp_eq_u32_e64 s[20:21], 5, v24
	v_cmp_eq_u32_e64 s[22:23], 0, v2
	v_cmp_eq_u32_e64 s[24:25], 1, v2
	v_cmp_eq_u32_e64 s[26:27], 2, v2
	v_cmp_eq_u32_e64 s[28:29], 3, v2
	s_and_b64 s[22:23], s[22:23], s[4:5]
	s_and_b64 s[24:25], s[24:25], s[4:5]
	s_and_b64 s[26:27], s[26:27], s[4:5]
	s_and_b64 s[28:29], s[28:29], s[4:5]
	v_mov_b32_e32 v71, 0xf149f2ca
	s_mov_b64 s[62:63], 0
	s_mov_b32 s69, 0xf149f2ca
	s_mov_b32 s70, 0xefa18f08
	s_mov_b32 s71, 0x41000000
	s_movk_i32 s72, 0x110
	s_mov_b32 s77, 0x26500
	s_mov_b32 s73, 0x2650c
	s_mov_b32 s80, -1
	s_mov_b32 s81, 0
	s_mov_b32 s82, 0
	s_mov_b32 s83, 0x7fffffff
	s_mov_b64 s[84:85], 0
	v_mov_b32_e32 v100, 0
	v_mov_b32_e32 v4, 0
	v_mov_b32_e32 v103, 0xf149f2ca
	v_mov_b32_e32 v46, v3
	v_mov_b32_e32 v47, v3
	v_mov_b32_e32 v48, v3
	v_mov_b32_e32 v49, v3
	v_mov_b32_e32 v50, v3
	v_mov_b32_e32 v51, v3
	v_mov_b32_e32 v52, v3
	v_mov_b32_e32 v53, v3
	v_mov_b32_e32 v38, v3
	v_mov_b32_e32 v39, v3
	v_mov_b32_e32 v40, v3
	v_mov_b32_e32 v41, v3
	v_mov_b32_e32 v42, v3
	v_mov_b32_e32 v43, v3
	v_mov_b32_e32 v44, v3
	v_mov_b32_e32 v45, v3
	v_mov_b32_e32 v30, v3
	v_mov_b32_e32 v31, v3
	v_mov_b32_e32 v32, v3
	v_mov_b32_e32 v33, v3
	v_mov_b32_e32 v34, v3
	v_mov_b32_e32 v35, v3
	v_mov_b32_e32 v36, v3
	v_mov_b32_e32 v37, v3
	v_mov_b32_e32 v22, v3
	v_mov_b32_e32 v23, v3
	v_mov_b32_e32 v24, v3
	v_mov_b32_e32 v25, v3
	v_mov_b32_e32 v26, v3
	v_mov_b32_e32 v28, v3
	v_mov_b32_e32 v29, v3
	v_readfirstlane_b32 s86, v80
	s_mov_b32 s87, 0
	v_readfirstlane_b32 s88, v99
	v_readfirstlane_b32 s89, v5
	v_readfirstlane_b32 s96, v54
	v_readfirstlane_b32 s97, v84
	v_readfirstlane_b32 s98, v85
	v_readfirstlane_b32 s99, v81
	v_readfirstlane_b32 s100, v83
	v_readfirstlane_b32 s101, v82
	s_cmp_ge_i32 s96, s68
	s_cselect_b32 s100, 0, s100
	v_readfirstlane_b32 s94, v0
	s_lshr_b32 s94, s94, 8
	s_cmp_eq_u32 s94, 0
	s_cbranch_scc1 .LBB0_95
.Lattn_stagger:
	s_sleep 37
	s_add_i32 s94, s94, -1
	s_cmp_lg_u32 s94, 0
	s_cbranch_scc1 .Lattn_stagger
	s_branch .LBB0_95
